# speedup vs baseline: 1.0427x; 1.0056x over previous
.LBB3_18:
	s_cmp_ge_u32 s46, 0x100
	s_cbranch_scc1 .Lst_b1
	v_mul_f32_e32 v6, 0xbe0293ee, v194
	v_mov_b32_e32 v195, v6
	s_addk_i32 s14, 0x80
	v_fmamk_f32 v5, v130, 0x3e0293ee, v6
	v_fmamk_f32 v7, v131, 0x3e0293ee, v6
	v_fmamk_f32 v8, v132, 0x3e0293ee, v6
	v_fmamk_f32 v9, v133, 0x3e0293ee, v6
	v_fmamk_f32 v10, v134, 0x3e0293ee, v6
	v_fmamk_f32 v11, v135, 0x3e0293ee, v6
	v_fmamk_f32 v12, v136, 0x3e0293ee, v6
	v_fmamk_f32 v13, v137, 0x3e0293ee, v6
	v_fmamk_f32 v14, v138, 0x3e0293ee, v6
	v_fmamk_f32 v15, v139, 0x3e0293ee, v6
	v_fmamk_f32 v16, v140, 0x3e0293ee, v6
	v_fmamk_f32 v17, v141, 0x3e0293ee, v6
	v_fmamk_f32 v130, v142, 0x3e0293ee, v6
	v_fmamk_f32 v132, v143, 0x3e0293ee, v6
	v_fmamk_f32 v135, v144, 0x3e0293ee, v6
	v_fmac_f32_e32 v195, 0x3e0293ee, v145
	s_add_u32 s30, s30, 0x8000
	v_exp_f32_e32 v143, v5
	v_exp_f32_e32 v145, v7
	v_exp_f32_e32 v141, v8
	v_exp_f32_e32 v144, v9
	v_exp_f32_e32 v140, v10
	v_exp_f32_e32 v142, v11
	v_exp_f32_e32 v138, v12
	v_exp_f32_e32 v139, v13
	v_exp_f32_e32 v133, v14
	v_exp_f32_e32 v136, v15
	v_exp_f32_e32 v131, v16
	v_exp_f32_e32 v134, v17
	v_exp_f32_e32 v130, v130
	v_exp_f32_e32 v137, v132
	v_exp_f32_e32 v132, v135
	v_exp_f32_e32 v135, v195
	s_addc_u32 s31, s31, 0
	v_add_f32_e32 v5, v222, v223
	s_add_u32 s28, s28, 0x8000
	v_fmac_f32_e32 v5, v219, v220
	v_add_f32_e32 v220, v224, v225
	s_addc_u32 s29, s29, 0
	s_add_i32 s51, s51, 2
	v_pk_fma_f32 v[128:129], v[128:129], s[18:19], v[6:7] op_sel_hi:[1,0,0]
	v_pk_fma_f32 v[126:127], v[126:127], s[18:19], v[6:7] op_sel_hi:[1,0,0]
	v_pk_fma_f32 v[124:125], v[124:125], s[18:19], v[6:7] op_sel_hi:[1,0,0]
	v_pk_fma_f32 v[122:123], v[122:123], s[18:19], v[6:7] op_sel_hi:[1,0,0]
	v_pk_fma_f32 v[120:121], v[120:121], s[18:19], v[6:7] op_sel_hi:[1,0,0]
	v_pk_fma_f32 v[118:119], v[118:119], s[18:19], v[6:7] op_sel_hi:[1,0,0]
	v_pk_fma_f32 v[116:117], v[116:117], s[18:19], v[6:7] op_sel_hi:[1,0,0]
	v_pk_fma_f32 v[114:115], v[114:115], s[18:19], v[6:7] op_sel_hi:[1,0,0]
	v_fmac_f32_e32 v220, v5, v2
	s_cmp_ge_i32 s51, s48
	v_add_u32_e32 v221, 0xffffff80, v221
	v_mov_b32_e32 v219, v4
	s_waitcnt lgkmcnt(0)
	s_barrier
	s_branch .Lst_b2
.Lst_b1:
	s_waitcnt lgkmcnt(0)
	s_barrier
	v_mul_f32_e32 v6, 0xbe0293ee, v194
	v_mov_b32_e32 v195, v6
	s_addk_i32 s14, 0x80
	v_fmamk_f32 v5, v130, 0x3e0293ee, v6
	v_fmamk_f32 v7, v131, 0x3e0293ee, v6
	v_fmamk_f32 v8, v132, 0x3e0293ee, v6
	v_fmamk_f32 v9, v133, 0x3e0293ee, v6
	v_fmamk_f32 v10, v134, 0x3e0293ee, v6
	v_fmamk_f32 v11, v135, 0x3e0293ee, v6
	v_fmamk_f32 v12, v136, 0x3e0293ee, v6
	v_fmamk_f32 v13, v137, 0x3e0293ee, v6
	v_fmamk_f32 v14, v138, 0x3e0293ee, v6
	v_fmamk_f32 v15, v139, 0x3e0293ee, v6
	v_fmamk_f32 v16, v140, 0x3e0293ee, v6
	v_fmamk_f32 v17, v141, 0x3e0293ee, v6
	v_fmamk_f32 v130, v142, 0x3e0293ee, v6
	v_fmamk_f32 v132, v143, 0x3e0293ee, v6
	v_fmamk_f32 v135, v144, 0x3e0293ee, v6
	v_fmac_f32_e32 v195, 0x3e0293ee, v145
	s_add_u32 s30, s30, 0x8000
	v_exp_f32_e32 v143, v5
	v_exp_f32_e32 v145, v7
	v_exp_f32_e32 v141, v8
	v_exp_f32_e32 v144, v9
	v_exp_f32_e32 v140, v10
	v_exp_f32_e32 v142, v11
	v_exp_f32_e32 v138, v12
	v_exp_f32_e32 v139, v13
	v_exp_f32_e32 v133, v14
	v_exp_f32_e32 v136, v15
	v_exp_f32_e32 v131, v16
	v_exp_f32_e32 v134, v17
	v_exp_f32_e32 v130, v130
	v_exp_f32_e32 v137, v132
	v_exp_f32_e32 v132, v135
	v_exp_f32_e32 v135, v195
	s_addc_u32 s31, s31, 0
	v_add_f32_e32 v5, v222, v223
	s_add_u32 s28, s28, 0x8000
	v_fmac_f32_e32 v5, v219, v220
	v_add_f32_e32 v220, v224, v225
	s_addc_u32 s29, s29, 0
	s_add_i32 s51, s51, 2
	v_pk_fma_f32 v[128:129], v[128:129], s[18:19], v[6:7] op_sel_hi:[1,0,0]
	v_pk_fma_f32 v[126:127], v[126:127], s[18:19], v[6:7] op_sel_hi:[1,0,0]
	v_pk_fma_f32 v[124:125], v[124:125], s[18:19], v[6:7] op_sel_hi:[1,0,0]
	v_pk_fma_f32 v[122:123], v[122:123], s[18:19], v[6:7] op_sel_hi:[1,0,0]
	v_pk_fma_f32 v[120:121], v[120:121], s[18:19], v[6:7] op_sel_hi:[1,0,0]
	v_pk_fma_f32 v[118:119], v[118:119], s[18:19], v[6:7] op_sel_hi:[1,0,0]
	v_pk_fma_f32 v[116:117], v[116:117], s[18:19], v[6:7] op_sel_hi:[1,0,0]
	v_pk_fma_f32 v[114:115], v[114:115], s[18:19], v[6:7] op_sel_hi:[1,0,0]
	v_fmac_f32_e32 v220, v5, v2
	s_cmp_ge_i32 s51, s48
	v_add_u32_e32 v221, 0xffffff80, v221
	v_mov_b32_e32 v219, v4
.Lst_b2:
	s_cmp_ge_i32 s51, s48
	s_cbranch_scc1 .Lattn_flush
.LBB3_19:
	ds_write_b128 v212, v[182:185] offset:16384
	ds_write_b128 v213, v[178:181] offset:16384
	ds_read_b128 v[4:7], v208 offset:49152
	ds_read_b128 v[8:11], v208 offset:49280
	v_exp_f32_e32 v2, v114
	v_exp_f32_e32 v16, v115
	v_exp_f32_e32 v17, v116
	s_waitcnt lgkmcnt(1)
	v_mfma_f32_32x32x16_f16 v[98:113], v[4:7], v[146:149], 0
	ds_read_b128 v[4:7], v208 offset:57344
	ds_read_b128 v[12:15], v208 offset:57472
	v_exp_f32_e32 v114, v117
	v_exp_f32_e32 v115, v118
	v_exp_f32_e32 v116, v119
	v_exp_f32_e32 v117, v120
	v_exp_f32_e32 v118, v121
	v_exp_f32_e32 v119, v122
	s_waitcnt lgkmcnt(1)
	v_mfma_f32_32x32x16_f16 v[82:97], v[4:7], v[146:149], 0
	ds_read_b128 v[4:7], v209 offset:49152
	s_waitcnt vmcnt(2)
	ds_read_b128 v[178:181], v209 offset:57344
	ds_read_b128 v[182:185], v209 offset:49280
	v_exp_f32_e32 v120, v123
	v_exp_f32_e32 v121, v124
	v_exp_f32_e32 v122, v125
	v_exp_f32_e32 v123, v126
	v_exp_f32_e32 v124, v127
	v_exp_f32_e32 v125, v128
	s_waitcnt lgkmcnt(2)
	v_mfma_f32_32x32x16_f16 v[98:113], v[4:7], v[150:153], v[98:113]
	s_waitcnt vmcnt(1)
	ds_read_b128 v[186:189], v209 offset:57472
	ds_read_b128 v[4:7], v210 offset:49152
	s_waitcnt vmcnt(0)
	ds_read_b128 v[190:193], v210 offset:49280
	ds_read_b128 v[222:225], v210 offset:57344
	ds_read_b128 v[226:229], v210 offset:57472
	ds_read_b128 v[230:233], v211 offset:49152
	ds_read_b128 v[234:237], v211 offset:49280
	v_exp_f32_e32 v126, v129
	s_waitcnt lgkmcnt(8)
	v_mfma_f32_32x32x16_f16 v[82:97], v[178:181], v[150:153], v[82:97]
	ds_read_b128 v[178:181], v211 offset:57344
	ds_read_b128 v[238:241], v211 offset:57472
	s_waitcnt lgkmcnt(7)
	v_mfma_f32_32x32x16_f16 v[98:113], v[4:7], v[154:157], v[98:113]
	v_add_f32_e32 v4, 0, v143
	v_add_f32_e32 v4, v145, v4
	v_add_f32_e32 v4, v141, v4
	v_add_f32_e32 v4, v144, v4
	v_add_f32_e32 v4, v140, v4
	v_add_f32_e32 v4, v142, v4
	v_add_f32_e32 v4, v138, v4
	s_waitcnt lgkmcnt(5)
	v_mfma_f32_32x32x16_f16 v[82:97], v[222:225], v[154:157], v[82:97]
	v_add_f32_e32 v4, v139, v4
	v_add_f32_e32 v4, v133, v4
	v_add_f32_e32 v4, v136, v4
	v_add_f32_e32 v4, v131, v4
	v_add_f32_e32 v4, v134, v4
	v_add_f32_e32 v4, v130, v4
	v_add_f32_e32 v4, v137, v4
	s_waitcnt lgkmcnt(3)
	v_mfma_f32_32x32x16_f16 v[98:113], v[230:233], v[158:161], v[98:113]
	v_add_f32_e32 v4, v132, v4
	v_add_f32_e32 v4, v135, v4
	v_add_f32_e32 v4, v2, v4
	v_add_f32_e32 v4, v16, v4
	v_add_f32_e32 v4, v17, v4
	v_add_f32_e32 v4, v114, v4
	v_add_f32_e32 v4, v115, v4
	s_waitcnt lgkmcnt(1)
	v_mfma_f32_32x32x16_f16 v[82:97], v[178:181], v[158:161], v[82:97]
	v_add_f32_e32 v4, v116, v4
	v_add_f32_e32 v4, v117, v4
	v_add_f32_e32 v4, v118, v4
	v_add_f32_e32 v4, v119, v4
	v_add_f32_e32 v4, v120, v4
	v_add_f32_e32 v4, v121, v4
	v_add_f32_e32 v4, v122, v4
	v_mfma_f32_32x32x16_f16 v[98:113], v[8:11], v[162:165], v[98:113]
	v_add_f32_e32 v4, v123, v4
	v_add_f32_e32 v4, v124, v4
	v_add_f32_e32 v4, v125, v4
	v_add_f32_e32 v222, v126, v4
	v_mov_b32_e32 v223, v222
	v_cvt_pk_f16_f32 v4, v143, v145
	v_cvt_pk_f16_f32 v5, v141, v144
	v_mfma_f32_32x32x16_f16 v[82:97], v[12:15], v[162:165], v[82:97]
	v_cvt_pk_f16_f32 v6, v140, v142
	v_cvt_pk_f16_f32 v7, v138, v139
	v_cvt_pk_f16_f32 v8, v133, v136
	v_cvt_pk_f16_f32 v9, v131, v134
	v_cvt_pk_f16_f32 v10, v130, v137
	v_cvt_pk_f16_f32 v11, v132, v135
	v_cvt_pk_f16_f32 v12, v2, v16
	v_mfma_f32_32x32x16_f16 v[98:113], v[182:185], v[166:169], v[98:113]
	v_cvt_pk_f16_f32 v13, v17, v114
	v_cvt_pk_f16_f32 v14, v115, v116
	v_cvt_pk_f16_f32 v15, v117, v118
	v_cvt_pk_f16_f32 v114, v119, v120
	v_cvt_pk_f16_f32 v115, v121, v122
	v_cvt_pk_f16_f32 v116, v123, v124
	v_cvt_pk_f16_f32 v117, v125, v126
	v_mfma_f32_32x32x16_f16 v[82:97], v[186:189], v[166:169], v[82:97]
	v_permlane32_swap_b32_e32 v222, v223
	v_permlane32_swap_b32_e32 v4, v6
	v_permlane32_swap_b32_e32 v5, v7
	v_permlane32_swap_b32_e32 v8, v10
	v_mfma_f32_32x32x16_f16 v[98:113], v[190:193], v[170:173], v[98:113]
	v_permlane32_swap_b32_e32 v9, v11
	v_permlane32_swap_b32_e32 v12, v14
	v_permlane32_swap_b32_e32 v13, v15
	v_permlane32_swap_b32_e32 v114, v116
	v_mfma_f32_32x32x16_f16 v[82:97], v[226:229], v[170:173], v[82:97]
	v_permlane32_swap_b32_e32 v115, v117
	v_mfma_f32_32x32x16_f16 v[98:113], v[234:237], v[174:177], v[98:113]
	s_waitcnt lgkmcnt(0)
	v_mfma_f32_32x32x16_f16 v[82:97], v[238:241], v[174:177], v[82:97]
	v_lshl_add_u64 v[204:205], s[30:31], 0, v[198:199]
	v_add_co_u32_e32 v16, vcc, s43, v204
	s_nop 1
	v_addc_co_u32_e32 v17, vcc, 0, v205, vcc
	v_add_co_u32_e32 v118, vcc, s44, v204
	s_nop 1
	v_addc_co_u32_e32 v119, vcc, 0, v205, vcc
	global_load_dwordx4 v[182:185], v[16:17], off
	global_load_dwordx4 v[178:181], v[118:119], off
	v_lshl_add_u64 v[16:17], s[28:29], 0, v[198:199]
	v_add_co_u32_e32 v118, vcc, s43, v16
	s_nop 1
	v_addc_co_u32_e32 v119, vcc, 0, v17, vcc
	v_add_co_u32_e32 v120, vcc, 0xa000, v16
	s_nop 1
	v_addc_co_u32_e32 v121, vcc, 0, v17, vcc
	global_load_dwordx4 v[186:189], v[118:119], off
	global_load_dwordx4 v[190:193], v[120:121], off
	s_add_i32 s34, s14, 0xffffff81
	s_sub_i32 s0, s14, 64
	s_cmp_le_i32 s0, s49
	s_cselect_b64 s[0:1], -1, 0
	s_cmp_gt_i32 s34, s50
	s_cselect_b64 s[34:35], -1, 0
	s_and_b64 s[0:1], s[34:35], s[0:1]
	s_and_b64 vcc, exec, s[0:1]
	s_cbranch_vccnz .LBB3_21
	v_add_u32_e32 v2, 0x87b, v221
	v_cmp_gt_u32_e32 vcc, s40, v2
	v_add_u32_e32 v2, 0x5b, v221
	s_nop 0
	v_cndmask_b32_e32 v98, v216, v98, vcc
	v_cmp_lt_u32_e32 vcc, s41, v2
	v_add_u32_e32 v2, 0x7a, v221
	s_nop 0
	v_cndmask_b32_e32 v82, v216, v82, vcc
	v_cmp_lt_u32_e32 vcc, s41, v2
	v_add_u32_e32 v2, 0x5a, v221
	s_nop 0
	v_cndmask_b32_e32 v99, v216, v99, vcc
	v_cmp_lt_u32_e32 vcc, s41, v2
	v_add_u32_e32 v2, 0x79, v221
	s_nop 0
	v_cndmask_b32_e32 v83, v216, v83, vcc
	v_cmp_lt_u32_e32 vcc, s41, v2
	v_add_u32_e32 v2, 0x59, v221
	s_nop 0
	v_cndmask_b32_e32 v100, v216, v100, vcc
	v_cmp_lt_u32_e32 vcc, s41, v2
	v_add_u32_e32 v2, 0x78, v221
	s_nop 0
	v_cndmask_b32_e32 v84, v216, v84, vcc
	v_cmp_lt_u32_e32 vcc, s41, v2
	v_add_u32_e32 v2, 0x58, v221
	s_nop 0
	v_cndmask_b32_e32 v101, v216, v101, vcc
	v_cmp_lt_u32_e32 vcc, s41, v2
	v_add_u32_e32 v2, 0x73, v221
	s_nop 0
	v_cndmask_b32_e32 v85, v216, v85, vcc
	v_cmp_lt_u32_e32 vcc, s41, v2
	v_add_u32_e32 v2, 0x53, v221
	s_nop 0
	v_cndmask_b32_e32 v102, v216, v102, vcc
	v_cmp_lt_u32_e32 vcc, s41, v2
	v_add_u32_e32 v2, 0x72, v221
	s_nop 0
	v_cndmask_b32_e32 v86, v216, v86, vcc
	v_cmp_lt_u32_e32 vcc, s41, v2
	v_add_u32_e32 v2, 0x52, v221
	s_nop 0
	v_cndmask_b32_e32 v103, v216, v103, vcc
	v_cmp_lt_u32_e32 vcc, s41, v2
	v_add_u32_e32 v2, 0x71, v221
	s_nop 0
	v_cndmask_b32_e32 v87, v216, v87, vcc
	v_cmp_lt_u32_e32 vcc, s41, v2
	v_add_u32_e32 v2, 0x51, v221
	s_nop 0
	v_cndmask_b32_e32 v104, v216, v104, vcc
	v_cmp_lt_u32_e32 vcc, s41, v2
	v_add_u32_e32 v2, 0x70, v221
	s_nop 0
	v_cndmask_b32_e32 v88, v216, v88, vcc
	v_cmp_lt_u32_e32 vcc, s41, v2
	v_add_u32_e32 v2, 0x50, v221
	s_nop 0
	v_cndmask_b32_e32 v105, v216, v105, vcc
	v_cmp_lt_u32_e32 vcc, s41, v2
	v_add_u32_e32 v2, 0x6b, v221
	s_nop 0
	v_cndmask_b32_e32 v89, v216, v89, vcc
	v_cmp_lt_u32_e32 vcc, s41, v2
	v_add_u32_e32 v2, 0x4b, v221
	s_nop 0
	v_cndmask_b32_e32 v106, v216, v106, vcc
	v_cmp_lt_u32_e32 vcc, s41, v2
	v_add_u32_e32 v2, 0x6a, v221
	s_nop 0
	v_cndmask_b32_e32 v90, v216, v90, vcc
	v_cmp_lt_u32_e32 vcc, s41, v2
	v_add_u32_e32 v2, 0x4a, v221
	s_nop 0
	v_cndmask_b32_e32 v107, v216, v107, vcc
	v_cmp_lt_u32_e32 vcc, s41, v2
	v_add_u32_e32 v2, 0x69, v221
	s_nop 0
	v_cndmask_b32_e32 v91, v216, v91, vcc
	v_cmp_lt_u32_e32 vcc, s41, v2
	v_add_u32_e32 v2, 0x49, v221
	s_nop 0
	v_cndmask_b32_e32 v108, v216, v108, vcc
	v_cmp_lt_u32_e32 vcc, s41, v2
	v_add_u32_e32 v2, 0x68, v221
	s_nop 0
	v_cndmask_b32_e32 v92, v216, v92, vcc
	v_cmp_lt_u32_e32 vcc, s41, v2
	v_add_u32_e32 v2, 0x48, v221
	s_nop 0
	v_cndmask_b32_e32 v109, v216, v109, vcc
	v_cmp_lt_u32_e32 vcc, s41, v2
	v_add_u32_e32 v2, 0x63, v221
	s_nop 0
	v_cndmask_b32_e32 v93, v216, v93, vcc
	v_cmp_lt_u32_e32 vcc, s41, v2
	v_add_u32_e32 v2, 0x43, v221
	s_nop 0
	v_cndmask_b32_e32 v110, v216, v110, vcc
	v_cmp_lt_u32_e32 vcc, s41, v2
	v_add_u32_e32 v2, 0x62, v221
	s_nop 0
	v_cndmask_b32_e32 v94, v216, v94, vcc
	v_cmp_lt_u32_e32 vcc, s41, v2
	v_add_u32_e32 v2, 0x42, v221
	s_nop 0
	v_cndmask_b32_e32 v111, v216, v111, vcc
	v_cmp_lt_u32_e32 vcc, s41, v2
	v_add_u32_e32 v2, 0x61, v221
	s_nop 0
	v_cndmask_b32_e32 v95, v216, v95, vcc
	v_cmp_lt_u32_e32 vcc, s41, v2
	v_add_u32_e32 v2, 0x41, v221
	s_nop 0
	v_cndmask_b32_e32 v112, v216, v112, vcc
	v_cmp_lt_u32_e32 vcc, s41, v2
	v_add_u32_e32 v2, 0x60, v221
	s_nop 0
	v_cndmask_b32_e32 v96, v216, v96, vcc
	v_cmp_lt_u32_e32 vcc, s41, v2
	v_add_u32_e32 v2, 64, v221
	s_nop 0
	v_cndmask_b32_e32 v113, v216, v113, vcc
	v_cmp_lt_u32_e32 vcc, s41, v2
	s_nop 1
	v_cndmask_b32_e32 v97, v216, v97, vcc
.LBB3_21:
	ds_read_b64_tr_b16 v[118:119], v207 offset:0
	ds_read_b64_tr_b16 v[120:121], v207 offset:0x800
	ds_read_b64_tr_b16 v[122:123], v207 offset:0x1000
	ds_read_b64_tr_b16 v[124:125], v207 offset:0x1800
	ds_read_b64_tr_b16 v[126:127], v207 offset:0x2000
	ds_read_b64_tr_b16 v[128:129], v207 offset:0x2800
	ds_read_b64_tr_b16 v[130:131], v207 offset:0x3000
	ds_read_b64_tr_b16 v[132:133], v207 offset:0x3800
	s_waitcnt lgkmcnt(0)
	s_nop 0
	v_mfma_f32_32x32x16_f16 v[66:81], v[118:121], v[4:7], v[66:81]
	v_max_f32_e32 v2, v99, v99
	v_max_f32_e32 v118, v98, v98
	v_max_f32_e32 v2, v118, v2
	v_max3_f32 v2, v2, v100, v101
	v_max3_f32 v2, v2, v102, v103
	v_max3_f32 v2, v2, v104, v105
	v_max3_f32 v2, v2, v106, v107
	v_mfma_f32_32x32x16_f16 v[66:81], v[122:125], v[8:11], v[66:81]
	v_max3_f32 v2, v2, v108, v109
	v_max3_f32 v2, v2, v110, v111
	v_max3_f32 v2, v2, v112, v113
	v_mfma_f32_32x32x16_f16 v[66:81], v[126:129], v[12:15], v[66:81]
	v_mfma_f32_32x32x16_f16 v[66:81], v[130:133], v[114:117], v[66:81]
	ds_read_b64_tr_b16 v[118:119], v207 offset:0x200
	ds_read_b64_tr_b16 v[120:121], v207 offset:0xa00
	ds_read_b64_tr_b16 v[122:123], v207 offset:0x1200
	ds_read_b64_tr_b16 v[124:125], v207 offset:0x1a00
	ds_read_b64_tr_b16 v[126:127], v207 offset:0x2200
	ds_read_b64_tr_b16 v[128:129], v207 offset:0x2a00
	ds_read_b64_tr_b16 v[130:131], v207 offset:0x3200
	ds_read_b64_tr_b16 v[132:133], v207 offset:0x3a00
	s_waitcnt lgkmcnt(0)
	s_nop 0
	v_mfma_f32_32x32x16_f16 v[50:65], v[118:121], v[4:7], v[50:65]
	v_max3_f32 v2, v2, v82, v83
	v_max3_f32 v2, v2, v84, v85
	v_max3_f32 v2, v2, v86, v87
	v_max3_f32 v2, v2, v88, v89
	v_max3_f32 v2, v2, v90, v91
	v_max3_f32 v2, v2, v92, v93
	v_max3_f32 v2, v2, v94, v95
	v_mfma_f32_32x32x16_f16 v[50:65], v[122:125], v[8:11], v[50:65]
	v_max3_f32 v2, v2, v96, v97
	v_mov_b32_e32 v118, v2
	s_nop 1
	v_permlane32_swap_b32_e32 v2, v118
	v_max_f32_e32 v118, v118, v118
	v_max_f32_e32 v2, v2, v2
	v_max_f32_e32 v2, v2, v118
	v_mfma_f32_32x32x16_f16 v[50:65], v[126:129], v[12:15], v[50:65]
	v_mfma_f32_32x32x16_f16 v[50:65], v[130:133], v[114:117], v[50:65]
	ds_read_b64_tr_b16 v[118:119], v207 offset:0x400
	ds_read_b64_tr_b16 v[120:121], v207 offset:0xc00
	ds_read_b64_tr_b16 v[122:123], v207 offset:0x1400
	ds_read_b64_tr_b16 v[124:125], v207 offset:0x1c00
	ds_read_b64_tr_b16 v[126:127], v207 offset:0x2400
	ds_read_b64_tr_b16 v[128:129], v207 offset:0x2c00
	ds_read_b64_tr_b16 v[130:131], v207 offset:0x3400
	ds_read_b64_tr_b16 v[132:133], v207 offset:0x3c00
	s_waitcnt lgkmcnt(0)
	s_nop 0
	v_mfma_f32_32x32x16_f16 v[34:49], v[118:121], v[4:7], v[34:49]
	v_sub_f32_e32 v118, v2, v194
	v_mul_f32_e32 v118, 0x3db504f3, v118
	v_cmp_ge_f32_e32 vcc, s42, v118
	s_cmp_eq_u64 vcc, exec
	v_max_f32_e32 v118, v194, v194
	v_max_f32_e32 v2, v118, v2
	s_cselect_b64 vcc, -1, 0
	v_mfma_f32_32x32x16_f16 v[34:49], v[122:125], v[8:11], v[34:49]
	v_cndmask_b32_e32 v226, v2, v194, vcc
	v_sub_f32_e32 v2, v194, v226
	v_mul_f32_e32 v2, 0x3e0293ee, v2
	v_exp_f32_e32 v2, v2
	s_nop 0
	v_cndmask_b32_e64 v2, v2, 1.0, vcc
	v_mfma_f32_32x32x16_f16 v[34:49], v[126:129], v[12:15], v[34:49]
	v_mfma_f32_32x32x16_f16 v[34:49], v[130:133], v[114:117], v[34:49]
	ds_read_b64_tr_b16 v[118:119], v207 offset:0x600
	ds_read_b64_tr_b16 v[120:121], v207 offset:0xe00
	ds_read_b64_tr_b16 v[122:123], v207 offset:0x1600
	ds_read_b64_tr_b16 v[124:125], v207 offset:0x1e00
	ds_read_b64_tr_b16 v[126:127], v207 offset:0x2600
	ds_read_b64_tr_b16 v[128:129], v207 offset:0x2e00
	ds_read_b64_tr_b16 v[130:131], v207 offset:0x3600
	ds_read_b64_tr_b16 v[132:133], v207 offset:0x3e00
	s_waitcnt lgkmcnt(0)
	s_nop 0
	v_mfma_f32_32x32x16_f16 v[18:33], v[118:121], v[4:7], v[18:33]
	v_mfma_f32_32x32x16_f16 v[18:33], v[122:125], v[8:11], v[18:33]
	v_mfma_f32_32x32x16_f16 v[18:33], v[126:129], v[12:15], v[18:33]
	v_mfma_f32_32x32x16_f16 v[18:33], v[130:133], v[114:117], v[18:33]
	s_waitcnt vmcnt(0)
	v_cmp_gt_f32_e32 vcc, 1.0, v2
	s_waitcnt vmcnt(1)
	ds_write_b128 v214, v[186:189] offset:32768
	s_waitcnt vmcnt(0)
	ds_write_b128 v214, v[190:193] offset:40960
	s_cmp_lt_u32 s59, s58
	s_cbranch_scc0 .Lwo_np_b
	v_cvt_pk_f16_f32 v246, v246, v247
	v_cvt_pk_f16_f32 v247, v248, v249
	v_cvt_pk_f16_f32 v248, v250, v251
	v_cvt_pk_f16_f32 v249, v252, v253
	s_lshl_b32 s61, s59, 13
	s_add_u32 s62, s56, s61
	s_addc_u32 s63, s57, 0
	global_store_dwordx4 v255, v[246:249], s[62:63]
	s_add_i32 s59, s59, 1

.LBB3_23:
	s_cmp_ge_u32 s46, 0x100
	s_cbranch_scc1 .Lst_a1
	v_mul_f32_e32 v12, 0xbe0293ee, v226
	v_fmamk_f32 v4, v98, 0x3e0293ee, v12
	v_fmamk_f32 v5, v99, 0x3e0293ee, v12
	v_fmamk_f32 v6, v100, 0x3e0293ee, v12
	v_fmamk_f32 v7, v101, 0x3e0293ee, v12
	v_fmamk_f32 v8, v102, 0x3e0293ee, v12
	v_fmamk_f32 v9, v103, 0x3e0293ee, v12
	v_fmamk_f32 v10, v104, 0x3e0293ee, v12
	v_fmamk_f32 v11, v105, 0x3e0293ee, v12
	v_fmamk_f32 v13, v106, 0x3e0293ee, v12
	v_fmamk_f32 v14, v107, 0x3e0293ee, v12
	v_fmamk_f32 v15, v108, 0x3e0293ee, v12
	v_fmamk_f32 v98, v109, 0x3e0293ee, v12
	v_fmamk_f32 v99, v110, 0x3e0293ee, v12
	v_fmamk_f32 v100, v111, 0x3e0293ee, v12
	v_fmamk_f32 v101, v112, 0x3e0293ee, v12
	v_fmamk_f32 v102, v113, 0x3e0293ee, v12
	v_fmamk_f32 v103, v82, 0x3e0293ee, v12
	v_fmamk_f32 v104, v83, 0x3e0293ee, v12
	v_fmamk_f32 v105, v84, 0x3e0293ee, v12
	v_fmamk_f32 v106, v85, 0x3e0293ee, v12
	v_fmamk_f32 v107, v86, 0x3e0293ee, v12
	v_fmamk_f32 v108, v87, 0x3e0293ee, v12
	v_fmamk_f32 v109, v88, 0x3e0293ee, v12
	v_fmamk_f32 v110, v89, 0x3e0293ee, v12
	v_fmamk_f32 v111, v90, 0x3e0293ee, v12
	v_fmamk_f32 v112, v91, 0x3e0293ee, v12
	v_fmamk_f32 v113, v92, 0x3e0293ee, v12
	v_fmamk_f32 v194, v93, 0x3e0293ee, v12
	v_fmamk_f32 v195, v94, 0x3e0293ee, v12
	v_fmamk_f32 v196, v95, 0x3e0293ee, v12
	v_fmamk_f32 v197, v96, 0x3e0293ee, v12
	v_fmac_f32_e32 v12, 0x3e0293ee, v97
	v_exp_f32_e32 v82, v4
	v_exp_f32_e32 v83, v5
	v_exp_f32_e32 v84, v6
	v_exp_f32_e32 v85, v7
	v_exp_f32_e32 v86, v8
	v_exp_f32_e32 v87, v9
	v_exp_f32_e32 v88, v10
	v_exp_f32_e32 v89, v11
	v_exp_f32_e32 v90, v13
	v_exp_f32_e32 v91, v14
	v_exp_f32_e32 v92, v15
	v_exp_f32_e32 v93, v98
	v_exp_f32_e32 v94, v99
	v_exp_f32_e32 v95, v100
	v_exp_f32_e32 v96, v101
	v_exp_f32_e32 v97, v102
	s_waitcnt lgkmcnt(0)
	s_barrier
	s_branch .Lst_a2
.Lst_a1:
	s_waitcnt lgkmcnt(0)
	s_barrier
	v_mul_f32_e32 v12, 0xbe0293ee, v226
	v_fmamk_f32 v4, v98, 0x3e0293ee, v12
	v_fmamk_f32 v5, v99, 0x3e0293ee, v12
	v_fmamk_f32 v6, v100, 0x3e0293ee, v12
	v_fmamk_f32 v7, v101, 0x3e0293ee, v12
	v_fmamk_f32 v8, v102, 0x3e0293ee, v12
	v_fmamk_f32 v9, v103, 0x3e0293ee, v12
	v_fmamk_f32 v10, v104, 0x3e0293ee, v12
	v_fmamk_f32 v11, v105, 0x3e0293ee, v12
	v_fmamk_f32 v13, v106, 0x3e0293ee, v12
	v_fmamk_f32 v14, v107, 0x3e0293ee, v12
	v_fmamk_f32 v15, v108, 0x3e0293ee, v12
	v_fmamk_f32 v98, v109, 0x3e0293ee, v12
	v_fmamk_f32 v99, v110, 0x3e0293ee, v12
	v_fmamk_f32 v100, v111, 0x3e0293ee, v12
	v_fmamk_f32 v101, v112, 0x3e0293ee, v12
	v_fmamk_f32 v102, v113, 0x3e0293ee, v12
	v_fmamk_f32 v103, v82, 0x3e0293ee, v12
	v_fmamk_f32 v104, v83, 0x3e0293ee, v12
	v_fmamk_f32 v105, v84, 0x3e0293ee, v12
	v_fmamk_f32 v106, v85, 0x3e0293ee, v12
	v_fmamk_f32 v107, v86, 0x3e0293ee, v12
	v_fmamk_f32 v108, v87, 0x3e0293ee, v12
	v_fmamk_f32 v109, v88, 0x3e0293ee, v12
	v_fmamk_f32 v110, v89, 0x3e0293ee, v12
	v_fmamk_f32 v111, v90, 0x3e0293ee, v12
	v_fmamk_f32 v112, v91, 0x3e0293ee, v12
	v_fmamk_f32 v113, v92, 0x3e0293ee, v12
	v_fmamk_f32 v194, v93, 0x3e0293ee, v12
	v_fmamk_f32 v195, v94, 0x3e0293ee, v12
	v_fmamk_f32 v196, v95, 0x3e0293ee, v12
	v_fmamk_f32 v197, v96, 0x3e0293ee, v12
	v_fmac_f32_e32 v12, 0x3e0293ee, v97
	v_exp_f32_e32 v82, v4
	v_exp_f32_e32 v83, v5
	v_exp_f32_e32 v84, v6
	v_exp_f32_e32 v85, v7
	v_exp_f32_e32 v86, v8
	v_exp_f32_e32 v87, v9
	v_exp_f32_e32 v88, v10
	v_exp_f32_e32 v89, v11
	v_exp_f32_e32 v90, v13
	v_exp_f32_e32 v91, v14
	v_exp_f32_e32 v92, v15
	v_exp_f32_e32 v93, v98
	v_exp_f32_e32 v94, v99
	v_exp_f32_e32 v95, v100
	v_exp_f32_e32 v96, v101
	v_exp_f32_e32 v97, v102
.Lst_a2:
	ds_write_b128 v212, v[182:185]
	ds_write_b128 v213, v[178:181]
	ds_read_b128 v[4:7], v208 offset:32768
	ds_read_b128 v[8:11], v208 offset:40960
	v_exp_f32_e32 v98, v103
	v_exp_f32_e32 v99, v104
	v_exp_f32_e32 v100, v105
	s_waitcnt lgkmcnt(1)
	v_mfma_f32_32x32x16_f16 v[130:145], v[4:7], v[146:149], 0
	v_exp_f32_e32 v101, v106
	v_exp_f32_e32 v102, v107
	v_exp_f32_e32 v103, v108
	v_exp_f32_e32 v104, v109
	v_exp_f32_e32 v105, v110
	v_exp_f32_e32 v106, v111
	v_exp_f32_e32 v107, v112
	s_waitcnt lgkmcnt(0)
	v_mfma_f32_32x32x16_f16 v[114:129], v[8:11], v[146:149], 0
	ds_read_b128 v[4:7], v209 offset:32768
	ds_read_b128 v[8:11], v209 offset:40960
	v_exp_f32_e32 v108, v113
	v_exp_f32_e32 v109, v194
	v_exp_f32_e32 v110, v195
	v_exp_f32_e32 v111, v196
	v_exp_f32_e32 v112, v197
	v_exp_f32_e32 v113, v12
	s_waitcnt lgkmcnt(1)
	v_mfma_f32_32x32x16_f16 v[130:145], v[4:7], v[150:153], v[130:145]
	s_waitcnt lgkmcnt(0)
	v_mfma_f32_32x32x16_f16 v[114:129], v[8:11], v[150:153], v[114:129]
	ds_read_b128 v[4:7], v210 offset:32768
	ds_read_b128 v[8:11], v210 offset:40960
	s_waitcnt lgkmcnt(1)
	v_mfma_f32_32x32x16_f16 v[130:145], v[4:7], v[154:157], v[130:145]
	s_waitcnt lgkmcnt(0)
	v_mfma_f32_32x32x16_f16 v[114:129], v[8:11], v[154:157], v[114:129]
	ds_read_b128 v[4:7], v211 offset:32768
	ds_read_b128 v[8:11], v211 offset:40960
	s_waitcnt lgkmcnt(1)
	v_mfma_f32_32x32x16_f16 v[130:145], v[4:7], v[158:161], v[130:145]
	s_waitcnt lgkmcnt(0)
	v_mfma_f32_32x32x16_f16 v[114:129], v[8:11], v[158:161], v[114:129]
	ds_read_b128 v[4:7], v208 offset:32896
	ds_read_b128 v[8:11], v208 offset:41088
	s_waitcnt lgkmcnt(1)
	v_mfma_f32_32x32x16_f16 v[130:145], v[4:7], v[162:165], v[130:145]
	s_waitcnt lgkmcnt(0)
	v_mfma_f32_32x32x16_f16 v[114:129], v[8:11], v[162:165], v[114:129]
	ds_read_b128 v[4:7], v209 offset:32896
	ds_read_b128 v[8:11], v209 offset:41088
	s_waitcnt lgkmcnt(1)
	v_mfma_f32_32x32x16_f16 v[130:145], v[4:7], v[166:169], v[130:145]
	s_waitcnt lgkmcnt(0)
	v_mfma_f32_32x32x16_f16 v[114:129], v[8:11], v[166:169], v[114:129]
	ds_read_b128 v[4:7], v210 offset:32896
	ds_read_b128 v[8:11], v210 offset:41088
	s_waitcnt lgkmcnt(1)
	v_mfma_f32_32x32x16_f16 v[130:145], v[4:7], v[170:173], v[130:145]
	s_waitcnt lgkmcnt(0)
	v_mfma_f32_32x32x16_f16 v[114:129], v[8:11], v[170:173], v[114:129]
	ds_read_b128 v[4:7], v211 offset:32896
	ds_read_b128 v[8:11], v211 offset:41088
	s_waitcnt lgkmcnt(1)
	v_mfma_f32_32x32x16_f16 v[130:145], v[4:7], v[174:177], v[130:145]
	v_add_f32_e32 v4, 0, v82
	v_add_f32_e32 v4, v83, v4
	v_add_f32_e32 v4, v84, v4
	v_add_f32_e32 v4, v85, v4
	v_add_f32_e32 v4, v86, v4
	v_add_f32_e32 v4, v87, v4
	v_add_f32_e32 v4, v88, v4
	v_add_f32_e32 v4, v89, v4
	v_add_f32_e32 v4, v90, v4
	v_add_f32_e32 v4, v91, v4
	v_add_f32_e32 v4, v92, v4
	v_add_f32_e32 v4, v93, v4
	v_add_f32_e32 v4, v94, v4
	v_add_f32_e32 v4, v95, v4
	v_add_f32_e32 v4, v96, v4
	v_add_f32_e32 v4, v97, v4
	v_add_f32_e32 v4, v98, v4
	v_add_f32_e32 v4, v99, v4
	v_add_f32_e32 v4, v100, v4
	v_add_f32_e32 v4, v101, v4
	v_add_f32_e32 v4, v102, v4
	v_add_f32_e32 v4, v103, v4
	v_add_f32_e32 v4, v104, v4
	v_add_f32_e32 v4, v105, v4
	v_add_f32_e32 v4, v106, v4
	v_add_f32_e32 v4, v107, v4
	s_waitcnt lgkmcnt(0)
	v_mfma_f32_32x32x16_f16 v[114:129], v[8:11], v[174:177], v[114:129]
	v_add_f32_e32 v4, v108, v4
	v_add_f32_e32 v4, v109, v4
	v_add_f32_e32 v4, v110, v4
	v_add_f32_e32 v4, v111, v4
	v_add_f32_e32 v4, v112, v4
	v_add_f32_e32 v224, v113, v4
	v_mov_b32_e32 v225, v224
	v_cvt_pk_f16_f32 v4, v82, v83
	v_cvt_pk_f16_f32 v5, v84, v85
	v_cvt_pk_f16_f32 v6, v86, v87
	v_cvt_pk_f16_f32 v7, v88, v89
	v_cvt_pk_f16_f32 v8, v90, v91
	v_cvt_pk_f16_f32 v9, v92, v93
	v_cvt_pk_f16_f32 v10, v94, v95
	v_cvt_pk_f16_f32 v11, v96, v97
	v_cvt_pk_f16_f32 v12, v98, v99
	v_cvt_pk_f16_f32 v13, v100, v101
	v_cvt_pk_f16_f32 v14, v102, v103
	v_cvt_pk_f16_f32 v15, v104, v105
	v_cvt_pk_f16_f32 v194, v106, v107
	v_cvt_pk_f16_f32 v195, v108, v109
	v_cvt_pk_f16_f32 v196, v110, v111
	v_cvt_pk_f16_f32 v197, v112, v113
	s_nop 1
	v_permlane32_swap_b32_e32 v224, v225
	v_permlane32_swap_b32_e32 v4, v6
	v_permlane32_swap_b32_e32 v5, v7
	v_permlane32_swap_b32_e32 v8, v10
	v_permlane32_swap_b32_e32 v9, v11
	v_permlane32_swap_b32_e32 v12, v14
	v_permlane32_swap_b32_e32 v13, v15
	v_permlane32_swap_b32_e32 v194, v196
	v_permlane32_swap_b32_e32 v195, v197
	s_add_i32 s0, s51, 1
	s_cmp_lt_i32 s0, s48
	s_cselect_b64 s[34:35], -1, 0
	s_cmp_ge_i32 s0, s48
	s_cbranch_scc1 .LBB3_25
	v_add_co_u32_e32 v178, vcc, 0xc000, v204
	s_nop 1
	v_addc_co_u32_e32 v179, vcc, 0, v205, vcc
	v_add_co_u32_e32 v180, vcc, 0xe000, v204
	s_nop 1
	v_addc_co_u32_e32 v181, vcc, 0, v205, vcc
	v_add_co_u32_e32 v186, vcc, 0xc000, v16
	global_load_dwordx4 v[182:185], v[178:179], off
	s_nop 0
	global_load_dwordx4 v[178:181], v[180:181], off
	v_addc_co_u32_e32 v187, vcc, 0, v17, vcc
	v_add_co_u32_e32 v16, vcc, 0xe000, v16
	s_nop 1
	v_addc_co_u32_e32 v17, vcc, 0, v17, vcc
	global_load_dwordx4 v[186:189], v[186:187], off
	s_nop 0
	global_load_dwordx4 v[190:193], v[16:17], off

.Lattn_flush:
	s_andn2_b64 vcc, exec, s[34:35]
	s_cbranch_vccnz .LBB3_32
	ds_write_b128 v212, v[182:185] offset:16384
	ds_write_b128 v213, v[178:181] offset:16384
	s_waitcnt lgkmcnt(0)
	s_barrier
	s_branch .LBB3_32
